# speedup vs baseline: 1.0070x; 1.0070x over previous
_Z13gemm64_kernelILi3ELi2ELb1ELi1EEv2GP:
	s_load_dwordx2 s[80:81], s[0:1], 0x50
	s_waitcnt lgkmcnt(0)
	s_load_dword s82, s[80:81], 0x0
	s_load_dword s83, s[80:81], 0x80
	s_load_dword s84, s[80:81], 0x100
	s_load_dword s85, s[80:81], 0x180
	s_load_dword s86, s[80:81], 0x200
	s_load_dword s87, s[80:81], 0x280
	s_load_dword s88, s[80:81], 0x300
	s_load_dword s89, s[80:81], 0x380
	s_load_dword s4, s[0:1], 0xb8
	s_load_dwordx2 s[12:13], s[0:1], 0x60
	s_load_dwordx4 s[8:11], s[0:1], 0x50
	s_waitcnt lgkmcnt(0)
	s_mul_i32 s7, s4, s3
	s_add_i32 s7, s7, s2
	s_and_b32 s6, s7, 7
	s_ashr_i32 s16, s7, 4
	s_cmp_lg_u32 s4, 16
	s_cbranch_scc0 .LBB9_2
	s_ashr_i32 s4, s7, 3
	s_lshl_b32 s3, s7, 1
	s_and_b32 s3, s3, 2
	s_and_b32 s5, s4, 1
	s_or_b32 s15, s3, s5
	s_mul_hi_i32 s3, s16, 0x38e38e39
	s_lshr_b32 s5, s3, 31
	s_ashr_i32 s3, s3, 3
	s_add_i32 s3, s3, s5
	s_mul_i32 s3, s3, 36
	s_sub_i32 s3, s16, s3
	s_lshl_b32 s3, s3, 2
	s_lshr_b32 s5, s6, 1
	s_mul_hi_i32 s4, s4, 0x38e38e39
	s_or_b32 s3, s3, s5
	s_lshr_b32 s5, s4, 31
	s_ashr_i32 s4, s4, 4
	s_add_i32 s14, s4, s5
	s_cbranch_execz .LBB9_3
	s_branch .LBB9_4

_Z13gemm64_kernelILi1ELi2ELb1ELi1EEv2GP:
	s_load_dwordx2 s[80:81], s[0:1], 0x50
	s_waitcnt lgkmcnt(0)
	s_load_dword s82, s[80:81], 0x0
	s_load_dword s83, s[80:81], 0x80
	s_load_dword s84, s[80:81], 0x100
	s_load_dword s85, s[80:81], 0x180
	s_load_dword s86, s[80:81], 0x200
	s_load_dword s87, s[80:81], 0x280
	s_load_dword s88, s[80:81], 0x300
	s_load_dword s89, s[80:81], 0x380
	s_load_dword s10, s[0:1], 0xb8
	s_load_dwordx2 s[8:9], s[0:1], 0x60
	s_load_dwordx4 s[4:7], s[0:1], 0x50
	s_waitcnt lgkmcnt(0)
	s_mul_i32 s13, s10, s3
	s_add_i32 s13, s13, s2
	s_and_b32 s12, s13, 7
	s_ashr_i32 s14, s13, 4
	s_cmp_lg_u32 s10, 16
	s_cbranch_scc0 .LBB10_2
	s_ashr_i32 s10, s13, 3
	s_lshl_b32 s3, s13, 1
	s_and_b32 s3, s3, 2
	s_and_b32 s11, s10, 1
	s_or_b32 s18, s3, s11
	s_mul_hi_i32 s3, s14, 0x38e38e39
	s_lshr_b32 s11, s3, 31
	s_ashr_i32 s3, s3, 3
	s_add_i32 s3, s3, s11
	s_mul_i32 s3, s3, 36
	s_sub_i32 s3, s14, s3
	s_lshl_b32 s3, s3, 2
	s_lshr_b32 s11, s12, 1
	s_mul_hi_i32 s10, s10, 0x38e38e39
	s_or_b32 s3, s3, s11
	s_lshr_b32 s11, s10, 31
	s_ashr_i32 s10, s10, 4
	s_add_i32 s19, s10, s11
	s_cbranch_execz .LBB10_3
	s_branch .LBB10_4

_Z13gemm64_kernelILi3ELi3ELb1ELi2EEv2GP:
	s_load_dwordx2 s[80:81], s[0:1], 0x50
	s_waitcnt lgkmcnt(0)
	s_load_dword s82, s[80:81], 0x0
	s_load_dword s83, s[80:81], 0x80
	s_load_dword s84, s[80:81], 0x100
	s_load_dword s85, s[80:81], 0x180
	s_load_dword s86, s[80:81], 0x200
	s_load_dword s87, s[80:81], 0x280
	s_load_dword s88, s[80:81], 0x300
	s_load_dword s89, s[80:81], 0x380
	s_load_dwordx2 s[16:17], s[0:1], 0xb8
	s_load_dwordx2 s[12:13], s[0:1], 0x60
	s_load_dwordx4 s[8:11], s[0:1], 0x50
	s_waitcnt lgkmcnt(0)
	s_mul_i32 s4, s17, s4
	s_add_i32 s3, s4, s3
	s_mul_i32 s7, s3, s16
	s_add_i32 s7, s7, s2
	s_and_b32 s6, s7, 7
	s_ashr_i32 s14, s7, 4
	s_cmp_lg_u32 s16, 16
	s_cbranch_scc0 .LBB12_2
	s_ashr_i32 s4, s7, 3
	s_lshl_b32 s3, s7, 1
	s_and_b32 s3, s3, 2
	s_and_b32 s5, s4, 1
	s_or_b32 s16, s3, s5
	s_mul_hi_i32 s3, s14, 0x38e38e39
	s_lshr_b32 s5, s3, 31
	s_ashr_i32 s3, s3, 3
	s_add_i32 s3, s3, s5
	s_mul_i32 s3, s3, 36
	s_sub_i32 s3, s14, s3
	s_lshl_b32 s3, s3, 2
	s_lshr_b32 s5, s6, 1
	s_mul_hi_i32 s4, s4, 0x38e38e39
	s_or_b32 s3, s3, s5
	s_lshr_b32 s5, s4, 31
	s_ashr_i32 s4, s4, 4
	s_add_i32 s22, s4, s5
	s_cbranch_execz .LBB12_3
	s_branch .LBB12_4

_Z13gemm64_kernelILi1ELi3ELb1ELi1EEv2GP:
	s_load_dwordx2 s[80:81], s[0:1], 0x50
	s_waitcnt lgkmcnt(0)
	s_load_dword s82, s[80:81], 0x0
	s_load_dword s83, s[80:81], 0x80
	s_load_dword s84, s[80:81], 0x100
	s_load_dword s85, s[80:81], 0x180
	s_load_dword s86, s[80:81], 0x200
	s_load_dword s87, s[80:81], 0x280
	s_load_dword s88, s[80:81], 0x300
	s_load_dword s89, s[80:81], 0x380
	s_load_dword s8, s[0:1], 0xb8
	s_load_dwordx2 s[12:13], s[0:1], 0x60
	s_load_dwordx4 s[4:7], s[0:1], 0x50
	s_waitcnt lgkmcnt(0)
	s_mul_i32 s11, s8, s3
	s_add_i32 s11, s11, s2
	s_and_b32 s10, s11, 7
	s_ashr_i32 s14, s11, 4
	s_cmp_lg_u32 s8, 16
	s_cbranch_scc0 .LBB13_2
	s_ashr_i32 s8, s11, 3
	s_lshl_b32 s3, s11, 1
	s_and_b32 s3, s3, 2
	s_and_b32 s9, s8, 1
	s_or_b32 s18, s3, s9
	s_mul_hi_i32 s3, s14, 0x38e38e39
	s_lshr_b32 s9, s3, 31
	s_ashr_i32 s3, s3, 3
	s_add_i32 s3, s3, s9
	s_mul_i32 s3, s3, 36
	s_sub_i32 s3, s14, s3
	s_lshl_b32 s3, s3, 2
	s_lshr_b32 s9, s10, 1
	s_mul_hi_i32 s8, s8, 0x38e38e39
	s_or_b32 s3, s3, s9
	s_lshr_b32 s9, s8, 31
	s_ashr_i32 s8, s8, 4
	s_add_i32 s19, s8, s9
	s_cbranch_execz .LBB13_3
	s_branch .LBB13_4
